# moe2 gemm2 K-loops: LDS-DMA prefetch distance raised from 2 to 3 K-tiles (stage of tile t+3 issued after the mid barrier of tile t into the 4th ring buffer, counted waits re-derived)
# baseline (speedup 1.0000x reference)
.LBB0_2448:
	s_or_b64 exec, exec, s[2:3]
	s_and_b32 s2, s1, 0xff
	s_mulk_i32 s2, 0xab
	s_lshr_b32 s4, s2, 8
	s_lshr_b32 s2, s2, 10
	s_mul_i32 s2, s2, 6
	s_sub_i32 s1, s1, s2
	s_and_b32 s49, s48, 3
	s_and_b32 s50, s1, 0xff
	s_cmp_lt_u32 s50, 5
	s_cselect_b32 s1, 1, 2
	s_cmp_lt_u32 s50, 3
	s_cselect_b64 s[20:21], -1, 0
	s_and_b64 s[2:3], s[20:21], exec
	s_cselect_b32 s1, 0, s1
	s_and_b32 s52, s4, 0xfc
	s_or_b32 s2, s1, s52
	s_ashr_i32 s1, s0, 31
	s_lshl_b64 s[0:1], s[0:1], 19
	s_add_u32 s4, s18, s0
	s_addc_u32 s5, s19, s1
	s_lshl_b32 s0, s2, 20
	s_add_u32 s0, s16, s0
	s_waitcnt lgkmcnt(0)
	s_barrier
	s_addc_u32 s1, s17, 0
	s_lshl_b32 s53, s49, 18
	s_mov_b32 s2, m0
	s_mov_b32 m0, s38
	s_nop 0
	global_load_lds_dwordx4 v184, s[4:5]
	s_mov_b32 m0, s2
	s_add_u32 s0, s0, s53
	s_mov_b32 s2, m0
	s_mov_b32 m0, s39
	s_nop 0
	global_load_lds_dwordx4 v185, s[4:5]
	s_mov_b32 m0, s2
	s_addc_u32 s1, s1, 0
	s_mov_b32 s2, m0
	s_mov_b32 m0, s40
	s_nop 0
	global_load_lds_dwordx4 v186, s[0:1]
	s_mov_b32 m0, s2
	s_nop 0
	s_mov_b32 s2, m0
	s_mov_b32 m0, s41
	s_nop 0
	global_load_lds_dwordx4 v187, s[0:1]
	s_mov_b32 m0, s2
	s_add_u32 s2, s4, 64
	s_addc_u32 s3, s5, 0
	s_mov_b32 s24, m0
	s_mov_b32 m0, s42
	s_nop 0
	global_load_lds_dwordx4 v184, s[2:3]
	s_mov_b32 m0, s24
	s_add_u32 s22, s0, 64
	s_mov_b32 s24, m0
	s_mov_b32 m0, s43
	s_nop 0
	global_load_lds_dwordx4 v185, s[2:3]
	s_mov_b32 m0, s24
	s_addc_u32 s23, s1, 0
	s_mov_b32 s2, m0
	s_mov_b32 m0, s44
	s_nop 0
	global_load_lds_dwordx4 v186, s[22:23]
	s_mov_b32 m0, s2
	s_and_b64 vcc, exec, s[12:13]
	s_mov_b32 s2, m0
	s_mov_b32 m0, s45
	s_nop 0
	global_load_lds_dwordx4 v187, s[22:23]
	s_mov_b32 m0, s2
	s_add_u32 s100, s4, 0x80
	s_addc_u32 s101, s5, 0
	s_mov_b32 s2, m0
	s_add_i32 m0, s37, 0x10000
	s_nop 0
	global_load_lds_dwordx4 v184, s[100:101]
	s_add_i32 m0, s37, 0x12000
	s_nop 0
	global_load_lds_dwordx4 v185, s[100:101]
	s_add_u32 s100, s0, 0x80
	s_addc_u32 s101, s1, 0
	s_add_i32 m0, s37, 0x14000
	s_nop 0
	global_load_lds_dwordx4 v186, s[100:101]
	s_add_i32 m0, s37, 0x16000
	s_nop 0
	global_load_lds_dwordx4 v187, s[100:101]
	s_mov_b32 m0, s2
	s_waitcnt vmcnt(8)
	s_barrier
	s_cbranch_vccz .LBB0_2450
	s_barrier
.LBB0_2450:
	s_add_u32 s22, s0, 0xc0
	s_addc_u32 s23, s1, 0
	s_add_u32 s24, s4, 0xc0
	v_mov_b32_e32 v4, 0
	s_addc_u32 s25, s5, 0
	s_mov_b32 s54, 0
	s_mov_b32 s55, 0
	v_mov_b64_e32 v[4:5], 0
	v_mov_b64_e32 v[6:7], 0
	v_mov_b64_e32 v[8:9], 0
	v_mov_b64_e32 v[10:11], 0
	v_mov_b64_e32 v[12:13], 0
	v_mov_b64_e32 v[14:15], 0
	v_mov_b64_e32 v[16:17], 0
	v_mov_b64_e32 v[18:19], 0
	v_mov_b64_e32 v[20:21], 0
	v_mov_b64_e32 v[22:23], 0
	v_mov_b64_e32 v[24:25], 0
	v_mov_b64_e32 v[26:27], 0
	v_mov_b64_e32 v[28:29], 0
	v_mov_b64_e32 v[30:31], 0
	v_mov_b64_e32 v[32:33], 0
	v_mov_b64_e32 v[34:35], 0
	v_mov_b64_e32 v[36:37], 0
	v_mov_b64_e32 v[38:39], 0
	v_mov_b64_e32 v[40:41], 0
	v_mov_b64_e32 v[42:43], 0
	v_mov_b64_e32 v[44:45], 0
	v_mov_b64_e32 v[46:47], 0
	v_mov_b64_e32 v[48:49], 0
	v_mov_b64_e32 v[50:51], 0
	v_mov_b64_e32 v[52:53], 0
	v_mov_b64_e32 v[54:55], 0
	v_mov_b64_e32 v[56:57], 0
	v_mov_b64_e32 v[58:59], 0
	v_mov_b64_e32 v[60:61], 0
	v_mov_b64_e32 v[62:63], 0
	v_mov_b64_e32 v[64:65], 0
	v_mov_b64_e32 v[66:67], 0
	v_mov_b64_e32 v[68:69], 0
	v_mov_b64_e32 v[70:71], 0
	v_mov_b64_e32 v[72:73], 0
	v_mov_b64_e32 v[74:75], 0
	v_mov_b64_e32 v[76:77], 0
	v_mov_b64_e32 v[78:79], 0
	v_mov_b64_e32 v[80:81], 0
	v_mov_b64_e32 v[82:83], 0
	v_mov_b64_e32 v[84:85], 0
	v_mov_b64_e32 v[86:87], 0
	v_mov_b64_e32 v[88:89], 0
	v_mov_b64_e32 v[90:91], 0
	v_mov_b64_e32 v[92:93], 0
	v_mov_b64_e32 v[94:95], 0
	v_mov_b64_e32 v[96:97], 0
	v_mov_b64_e32 v[98:99], 0
	v_mov_b64_e32 v[100:101], 0
	v_mov_b64_e32 v[102:103], 0
	v_mov_b64_e32 v[104:105], 0
	v_mov_b64_e32 v[106:107], 0
	v_mov_b64_e32 v[108:109], 0
	v_mov_b64_e32 v[110:111], 0
	v_mov_b64_e32 v[112:113], 0
	v_mov_b64_e32 v[114:115], 0
	v_mov_b64_e32 v[116:117], 0
	v_mov_b64_e32 v[118:119], 0
	v_mov_b64_e32 v[120:121], 0
	v_mov_b64_e32 v[122:123], 0
	v_mov_b64_e32 v[124:125], 0
	v_mov_b64_e32 v[126:127], 0
	v_mov_b64_e32 v[128:129], 0
	v_mov_b64_e32 v[130:131], 0
	s_branch .LBB0_2452

.LBB0_2452:
	s_cmp_gt_u32 s54, 13
	s_cselect_b64 s[26:27], -1, 0
.LBB0_2454:
	s_lshl_b32 s0, s55, 15
	s_add_i32 s0, s0, 0
	v_add_u32_e32 v2, s0, v182
	ds_read_b128 v[140:143], v2 offset:16384
	ds_read_b128 v[144:147], v2 offset:17408
	ds_read_b128 v[136:139], v2 offset:18432
	ds_read_b128 v[132:135], v2 offset:19456
	v_add_u32_e32 v2, s0, v181
	ds_read_b128 v[176:179], v2
	ds_read_b128 v[172:175], v2 offset:1024
	ds_read_b128 v[168:171], v2 offset:2048
	ds_read_b128 v[164:167], v2 offset:3072
	ds_read_b128 v[160:163], v2 offset:4096
	ds_read_b128 v[156:159], v2 offset:5120
	ds_read_b128 v[152:155], v2 offset:6144
	ds_read_b128 v[148:151], v2 offset:7168
	v_cndmask_b32_e64 v2, 0, 1, s[12:13]
	v_cmp_ne_u32_e64 s[0:1], 1, v2
	s_andn2_b64 vcc, exec, s[12:13]
	s_cbranch_vccnz .LBB0_2459
	s_mov_b64 s[2:3], -1
	s_and_b64 vcc, exec, s[26:27]
	s_cbranch_vccz .LBB0_2457
	s_waitcnt vmcnt(0)
	s_mov_b64 s[2:3], 0

.LBB0_2459:
	s_waitcnt lgkmcnt(7)
	v_mfma_f32_16x16x32_bf16 v[128:131], v[140:143], v[176:179], v[128:131]
	s_barrier
	s_cmp_gt_u32 s54, 12
	s_cbranch_scc1 .Lmy_g2a_nostage
	s_add_i32 s100, s55, 3
	s_and_b32 s100, s100, 3
	s_lshl_b32 s100, s100, 15
	s_add_i32 s100, s37, s100
	s_mov_b32 s101, m0
	s_mov_b32 m0, s100
	s_nop 0
	global_load_lds_dwordx4 v184, s[24:25]
	s_add_i32 m0, s100, 0x2000
	s_nop 0
	global_load_lds_dwordx4 v185, s[24:25]
	s_add_i32 m0, s100, 0x4000
	s_nop 0
	global_load_lds_dwordx4 v186, s[22:23]
	s_add_i32 m0, s100, 0x6000
	s_nop 0
	global_load_lds_dwordx4 v187, s[22:23]
	s_mov_b32 m0, s101
.Lmy_g2a_nostage:
	v_cndmask_b32_e64 v2, 0, 1, s[14:15]
	v_mfma_f32_16x16x32_bf16 v[124:127], v[144:147], v[176:179], v[124:127]
	v_cmp_ne_u32_e64 s[2:3], 1, v2
	s_andn2_b64 vcc, exec, s[14:15]
	v_mfma_f32_16x16x32_bf16 v[120:123], v[136:139], v[176:179], v[120:123]
	v_mfma_f32_16x16x32_bf16 v[116:119], v[132:135], v[176:179], v[116:119]
	s_waitcnt lgkmcnt(6)
	v_mfma_f32_16x16x32_bf16 v[112:115], v[140:143], v[172:175], v[112:115]
	v_mfma_f32_16x16x32_bf16 v[108:111], v[144:147], v[172:175], v[108:111]
	v_mfma_f32_16x16x32_bf16 v[104:107], v[136:139], v[172:175], v[104:107]
	v_mfma_f32_16x16x32_bf16 v[100:103], v[132:135], v[172:175], v[100:103]
	s_waitcnt lgkmcnt(5)
	v_mfma_f32_16x16x32_bf16 v[96:99], v[140:143], v[168:171], v[96:99]
	v_mfma_f32_16x16x32_bf16 v[92:95], v[144:147], v[168:171], v[92:95]
	v_mfma_f32_16x16x32_bf16 v[88:91], v[136:139], v[168:171], v[88:91]
	v_mfma_f32_16x16x32_bf16 v[84:87], v[132:135], v[168:171], v[84:87]
	s_waitcnt lgkmcnt(4)
	v_mfma_f32_16x16x32_bf16 v[80:83], v[140:143], v[164:167], v[80:83]
	v_mfma_f32_16x16x32_bf16 v[76:79], v[144:147], v[164:167], v[76:79]
	v_mfma_f32_16x16x32_bf16 v[72:75], v[136:139], v[164:167], v[72:75]
	v_mfma_f32_16x16x32_bf16 v[68:71], v[132:135], v[164:167], v[68:71]
	s_waitcnt lgkmcnt(3)
	v_mfma_f32_16x16x32_bf16 v[64:67], v[140:143], v[160:163], v[64:67]
	v_mfma_f32_16x16x32_bf16 v[60:63], v[144:147], v[160:163], v[60:63]
	v_mfma_f32_16x16x32_bf16 v[56:59], v[136:139], v[160:163], v[56:59]
	v_mfma_f32_16x16x32_bf16 v[52:55], v[132:135], v[160:163], v[52:55]
	s_waitcnt lgkmcnt(2)
	v_mfma_f32_16x16x32_bf16 v[48:51], v[140:143], v[156:159], v[48:51]
	v_mfma_f32_16x16x32_bf16 v[44:47], v[144:147], v[156:159], v[44:47]
	v_mfma_f32_16x16x32_bf16 v[40:43], v[136:139], v[156:159], v[40:43]
	v_mfma_f32_16x16x32_bf16 v[36:39], v[132:135], v[156:159], v[36:39]
	s_waitcnt lgkmcnt(1)
	v_mfma_f32_16x16x32_bf16 v[32:35], v[140:143], v[152:155], v[32:35]
	v_mfma_f32_16x16x32_bf16 v[28:31], v[144:147], v[152:155], v[28:31]
	v_mfma_f32_16x16x32_bf16 v[24:27], v[136:139], v[152:155], v[24:27]
	v_mfma_f32_16x16x32_bf16 v[20:23], v[132:135], v[152:155], v[20:23]
	s_waitcnt lgkmcnt(0)
	v_mfma_f32_16x16x32_bf16 v[16:19], v[140:143], v[148:151], v[16:19]
	v_mfma_f32_16x16x32_bf16 v[12:15], v[144:147], v[148:151], v[12:15]
	v_mfma_f32_16x16x32_bf16 v[8:11], v[136:139], v[148:151], v[8:11]
	v_mfma_f32_16x16x32_bf16 v[4:7], v[132:135], v[148:151], v[4:7]
	s_cbranch_vccnz .LBB0_2451
	s_mov_b64 s[28:29], -1
	s_and_b64 vcc, exec, s[26:27]
	s_cbranch_vccz .LBB0_2462
	s_waitcnt vmcnt(0)
	s_mov_b64 s[28:29], 0
.LBB0_2462:
	s_andn2_b64 vcc, exec, s[28:29]
	s_cbranch_vccnz .LBB0_2451
	s_cmp_gt_u32 s54, 12
	s_cbranch_scc1 .Lmy_g2a_w4
	s_waitcnt vmcnt(8)
	s_branch .LBB0_2451
.Lmy_g2a_w4:
	s_waitcnt vmcnt(4)
	s_branch .LBB0_2451

.LBB0_2466:
	s_min_u32 s23, s50, 4
	s_add_i32 s22, s50, 1
	s_add_i32 s23, s23, -1
	s_and_b64 s[20:21], s[20:21], exec
	s_cselect_b32 s20, s22, s23
	s_add_i32 s22, s20, s52
	s_add_u32 s20, s4, 0x400
	s_addc_u32 s21, s5, 0
	s_ashr_i32 s23, s22, 31
	s_lshl_b64 s[22:23], s[22:23], 20
	v_mov_b32_e32 v2, v180
	s_add_u32 s22, s16, s22
	s_addc_u32 s23, s17, s23
	s_mov_b32 s24, m0
	s_mov_b32 m0, s38
	s_nop 0
	global_load_lds_dwordx4 v184, s[20:21]
	s_mov_b32 m0, s24
	s_add_u32 s22, s22, s53
	s_mov_b32 s24, m0
	s_mov_b32 m0, s39
	s_nop 0
	global_load_lds_dwordx4 v185, s[20:21]
	s_mov_b32 m0, s24
	s_addc_u32 s23, s23, 0
	s_mov_b32 s24, m0
	s_mov_b32 m0, s40
	s_nop 0
	global_load_lds_dwordx4 v186, s[22:23]
	s_mov_b32 m0, s24
	s_add_u32 s4, s4, 0x440
	s_mov_b32 s24, m0
	s_mov_b32 m0, s41
	s_nop 0
	global_load_lds_dwordx4 v187, s[22:23]
	s_mov_b32 m0, s24
	s_addc_u32 s5, s5, 0
	s_mov_b32 s26, m0
	s_mov_b32 m0, s42
	s_nop 0
	global_load_lds_dwordx4 v184, s[4:5]
	s_mov_b32 m0, s26
	s_add_u32 s24, s22, 64
	s_mov_b32 s26, m0
	s_mov_b32 m0, s43
	s_nop 0
	global_load_lds_dwordx4 v185, s[4:5]
	s_mov_b32 m0, s26
	s_addc_u32 s25, s23, 0
	s_mov_b32 s4, m0
	s_mov_b32 m0, s44
	s_nop 0
	global_load_lds_dwordx4 v186, s[24:25]
	s_mov_b32 m0, s4
	s_and_b64 vcc, exec, s[12:13]
	s_mov_b32 s4, m0
	s_mov_b32 m0, s45
	s_nop 0
	global_load_lds_dwordx4 v187, s[24:25]
	s_mov_b32 m0, s4
	s_add_u32 s100, s20, 0x80
	s_addc_u32 s101, s21, 0
	s_mov_b32 s26, m0
	s_add_i32 m0, s37, 0x10000
	s_nop 0
	global_load_lds_dwordx4 v184, s[100:101]
	s_add_i32 m0, s37, 0x12000
	s_nop 0
	global_load_lds_dwordx4 v185, s[100:101]
	s_add_u32 s100, s22, 0x80
	s_addc_u32 s101, s23, 0
	s_add_i32 m0, s37, 0x14000
	s_nop 0
	global_load_lds_dwordx4 v186, s[100:101]
	s_add_i32 m0, s37, 0x16000
	s_nop 0
	global_load_lds_dwordx4 v187, s[100:101]
	s_mov_b32 m0, s26
	s_waitcnt vmcnt(8)
	s_barrier
	s_cbranch_vccz .LBB0_2468
	s_barrier
.LBB0_2468:
	s_add_u32 s4, s22, 0xc0
	s_addc_u32 s5, s23, 0
	s_add_u32 s20, s20, 0xc0
	s_addc_u32 s21, s21, 0
	s_mov_b32 s26, 0
	s_mov_b32 s27, 0
	s_branch .LBB0_2470

.LBB0_2470:
	s_cmp_gt_u32 s26, 13
	s_cselect_b64 s[22:23], -1, 0
.LBB0_2472:
	s_lshl_b32 s24, s27, 15
	s_add_i32 s24, s24, 0
	v_add_u32_e32 v2, s24, v182
	ds_read_b128 v[136:139], v2 offset:16384
	ds_read_b128 v[140:143], v2 offset:17408
	ds_read_b128 v[144:147], v2 offset:18432
	ds_read_b128 v[132:135], v2 offset:19456
	v_add_u32_e32 v2, s24, v181
	ds_read_b128 v[176:179], v2
	ds_read_b128 v[172:175], v2 offset:1024
	ds_read_b128 v[168:171], v2 offset:2048
	ds_read_b128 v[164:167], v2 offset:3072
	ds_read_b128 v[160:163], v2 offset:4096
	ds_read_b128 v[156:159], v2 offset:5120
	ds_read_b128 v[152:155], v2 offset:6144
	ds_read_b128 v[148:151], v2 offset:7168
	s_and_b64 vcc, exec, s[0:1]
	s_cbranch_vccnz .LBB0_2477
	s_mov_b64 s[24:25], -1
	s_and_b64 vcc, exec, s[22:23]
	s_cbranch_vccz .LBB0_2475
	s_waitcnt vmcnt(0)
	s_mov_b64 s[24:25], 0

.LBB0_2477:
	s_waitcnt lgkmcnt(7)
	v_mfma_f32_16x16x32_bf16 v[128:131], v[136:139], v[176:179], v[128:131]
	s_barrier
	s_cmp_gt_u32 s26, 12
	s_cbranch_scc1 .Lmy_g2b_nostage
	s_add_i32 s100, s27, 3
	s_and_b32 s100, s100, 3
	s_lshl_b32 s100, s100, 15
	s_add_i32 s100, s37, s100
	s_mov_b32 s101, m0
	s_mov_b32 m0, s100
	s_nop 0
	global_load_lds_dwordx4 v184, s[20:21]
	s_add_i32 m0, s100, 0x2000
	s_nop 0
	global_load_lds_dwordx4 v185, s[20:21]
	s_add_i32 m0, s100, 0x4000
	s_nop 0
	global_load_lds_dwordx4 v186, s[4:5]
	s_add_i32 m0, s100, 0x6000
	s_nop 0
	global_load_lds_dwordx4 v187, s[4:5]
	s_mov_b32 m0, s101
.Lmy_g2b_nostage:
	s_and_b64 vcc, exec, s[2:3]
	v_mfma_f32_16x16x32_bf16 v[124:127], v[140:143], v[176:179], v[124:127]
	v_mfma_f32_16x16x32_bf16 v[120:123], v[144:147], v[176:179], v[120:123]
	v_mfma_f32_16x16x32_bf16 v[116:119], v[132:135], v[176:179], v[116:119]
	s_waitcnt lgkmcnt(6)
	v_mfma_f32_16x16x32_bf16 v[112:115], v[136:139], v[172:175], v[112:115]
	v_mfma_f32_16x16x32_bf16 v[108:111], v[140:143], v[172:175], v[108:111]
	v_mfma_f32_16x16x32_bf16 v[104:107], v[144:147], v[172:175], v[104:107]
	v_mfma_f32_16x16x32_bf16 v[100:103], v[132:135], v[172:175], v[100:103]
	s_waitcnt lgkmcnt(5)
	v_mfma_f32_16x16x32_bf16 v[96:99], v[136:139], v[168:171], v[96:99]
	v_mfma_f32_16x16x32_bf16 v[92:95], v[140:143], v[168:171], v[92:95]
	v_mfma_f32_16x16x32_bf16 v[88:91], v[144:147], v[168:171], v[88:91]
	v_mfma_f32_16x16x32_bf16 v[84:87], v[132:135], v[168:171], v[84:87]
	s_waitcnt lgkmcnt(4)
	v_mfma_f32_16x16x32_bf16 v[80:83], v[136:139], v[164:167], v[80:83]
	v_mfma_f32_16x16x32_bf16 v[76:79], v[140:143], v[164:167], v[76:79]
	v_mfma_f32_16x16x32_bf16 v[72:75], v[144:147], v[164:167], v[72:75]
	v_mfma_f32_16x16x32_bf16 v[68:71], v[132:135], v[164:167], v[68:71]
	s_waitcnt lgkmcnt(3)
	v_mfma_f32_16x16x32_bf16 v[64:67], v[136:139], v[160:163], v[64:67]
	v_mfma_f32_16x16x32_bf16 v[60:63], v[140:143], v[160:163], v[60:63]
	v_mfma_f32_16x16x32_bf16 v[56:59], v[144:147], v[160:163], v[56:59]
	v_mfma_f32_16x16x32_bf16 v[52:55], v[132:135], v[160:163], v[52:55]
	s_waitcnt lgkmcnt(2)
	v_mfma_f32_16x16x32_bf16 v[48:51], v[136:139], v[156:159], v[48:51]
	v_mfma_f32_16x16x32_bf16 v[44:47], v[140:143], v[156:159], v[44:47]
	v_mfma_f32_16x16x32_bf16 v[40:43], v[144:147], v[156:159], v[40:43]
	v_mfma_f32_16x16x32_bf16 v[36:39], v[132:135], v[156:159], v[36:39]
	s_waitcnt lgkmcnt(1)
	v_mfma_f32_16x16x32_bf16 v[32:35], v[136:139], v[152:155], v[32:35]
	v_mfma_f32_16x16x32_bf16 v[28:31], v[140:143], v[152:155], v[28:31]
	v_mfma_f32_16x16x32_bf16 v[24:27], v[144:147], v[152:155], v[24:27]
	v_mfma_f32_16x16x32_bf16 v[20:23], v[132:135], v[152:155], v[20:23]
	s_waitcnt lgkmcnt(0)
	v_mfma_f32_16x16x32_bf16 v[16:19], v[136:139], v[148:151], v[16:19]
	v_mfma_f32_16x16x32_bf16 v[12:15], v[140:143], v[148:151], v[12:15]
	v_mfma_f32_16x16x32_bf16 v[8:11], v[144:147], v[148:151], v[8:11]
	v_mfma_f32_16x16x32_bf16 v[4:7], v[132:135], v[148:151], v[4:7]
	s_cbranch_vccnz .LBB0_2469
	s_mov_b64 s[24:25], -1
	s_and_b64 vcc, exec, s[22:23]
	s_cbranch_vccz .LBB0_2480
	s_waitcnt vmcnt(0)
	s_mov_b64 s[24:25], 0
.LBB0_2480:
	s_andn2_b64 vcc, exec, s[24:25]
	s_cbranch_vccnz .LBB0_2469
	s_cmp_gt_u32 s26, 12
	s_cbranch_scc1 .Lmy_g2b_w4
	s_waitcnt vmcnt(8)
	s_branch .LBB0_2469
